# grid barrier polling cadence: s_sleep 32 instead of s_sleep 1 between polls of the generation word (fewer reads competing with the generation update)
# baseline (speedup 1.0000x reference)
.LBB0_70:
	s_and_b32 s1, s0, 0xff
	s_mov_b64 s[20:21], -1
	s_cmp_lg_u32 s1, 0
	s_mov_b64 s[28:29], -1
	s_sleep 32
	s_cbranch_scc0 .LBB0_73
	s_and_b64 vcc, exec, s[28:29]
	s_cbranch_vccz .LBB0_69

.LBB0_87:
	s_and_b32 s1, s0, 0xff
	s_cmp_lg_u32 s1, 0
	s_mov_b64 s[22:23], -1
	s_sleep 32
	s_cbranch_scc0 .LBB0_90
	s_mov_b64 s[28:29], -1
	s_and_b64 vcc, exec, s[22:23]
	s_cbranch_vccz .LBB0_86
